# LN1 row loop: the 12 modulation-vector loads per row are cached in registers and re-loaded only when the row's sample changes (every second row of a wave)
# speedup vs baseline: 1.0085x; 1.0085x over previous
; #define GAS __attribute__((address_space(1)))
; __device__ __forceinline__ void unpack8(const u32x4 q, float* o) { o[0] = bflo(q.x); o[1] = bfhi(q.x); o[2] = bflo(q.y); o[3] = bfhi(q.y); o[4] = bflo(q.z); o[5] = bfhi(q.z); o[6] = bflo(q.w); o[7] = bfhi(q.w); }
; __device__ __forceinline__ void ph_ln1(Frame& F, int l, int ntok) {
;     const int gw = F.wg * NWAVES + F.wave, NGW = F.G * NWAVES;
;     const int cA = 256 * (F.lane >> 4) + 32 * ((F.lane >> 2) & 3) + 8 * (F.lane & 3);
;     ...
;     const float* lg = F.in[I_LN1G] + l * DM; const float* lb = F.in[I_LN1B] + l * DM;
;     for (int row = gw; row < ntok; row += NGW) {
;         bf16_t* xr = (bf16_t*)(F.ws + WS_XR) + (size_t)row * DM;
;         const unsigned char* yr = (const unsigned char*)(F.ws + WS_Y) + (size_t)row * DM + 16 * F.lane;
;         const float* md = mod_ptr(F, l, row);
;         const u32x4 xa = __builtin_nontemporal_load((const GAS u32x4*)(xr + cA)), xb = __builtin_nontemporal_load((const GAS u32x4*)(xr + cA + 128)), ya = __builtin_nontemporal_load((const GAS u32x4*)yr);
;         float x[16], y[16], v[16]; unpack8(xa, x); unpack8(xb, x + 8);
;         { const unsigned a[4] = {ya.x, ya.y, ya.z, ya.w};
; #pragma unroll
;           for (int e = 0; e < 4; ++e) { const f32x2 lo = __builtin_amdgcn_cvt_pk_f32_fp8((int)a[e], false), hi = __builtin_amdgcn_cvt_pk_f32_fp8((int)a[e], true); y[4 * e] = lo.x; y[4 * e + 1] = lo.y; y[4 * e + 2] = hi.x; y[4 * e + 3] = hi.y; } }
;         float s = 0.f;
; #pragma unroll
;         for (int j = 0; j < 4; ++j) { const f32x4 g1 = *(const GAS f32x4*)(md + 2048 + LN1_COL(j));
; #pragma unroll
;             for (int e = 0; e < 4; ++e) { v[4 * j + e] = x[4 * j + e] * DN_ALPHA + g1[e] * y[4 * j + e]; s += v[4 * j + e]; } }
;         const float mean = wave_sum(s, F.lane) * (1.f / DM); float s2 = 0.f;
; #pragma unroll
;         for (int e = 0; e < 16; ++e) { v[e] -= mean; s2 += v[e] * v[e]; }
;         const float rstd = 1.f / sqrtf(wave_sum(s2, F.lane) * (1.f / DM) + LN_EPS);
;         unsigned wx[8]; int w8[4];
; #pragma unroll
;         for (int j = 0; j < 4; ++j) { const f32x4 g = *(const GAS f32x4*)(lg + LN1_COL(j)), bb = *(const GAS f32x4*)(lb + LN1_COL(j)), sh = *(const GAS f32x4*)(md + 3072 + LN1_COL(j)), sc = *(const GAS f32x4*)(md + 4096 + LN1_COL(j));
.LBB0_772:
	s_andn2_b64 vcc, exec, s[2:3]
	s_cbranch_vccnz .LBB0_826
	v_readlane_b32 s36, v252, 8
	v_readlane_b32 s37, v252, 9
	s_mov_b32 s0, s97
	v_readlane_b32 s38, v252, 10
	v_readlane_b32 s39, v252, 11
	s_mov_b64 s[2:3], s[36:37]
	v_mbcnt_lo_u32_b32 v0, -1, 0
	v_mbcnt_hi_u32_b32 v0, -1, v0
	v_readlane_b32 s8, v255, 14
	v_readlane_b32 s2, v254, 28
	s_add_i32 s40, s0, s2
	v_readlane_b32 s9, v255, 15
	v_readlane_b32 s10, v255, 3
	v_readlane_b32 s18, v255, 5
	s_cmp_ge_i32 s40, s80
	v_readlane_b32 s11, v255, 4
	v_readlane_b32 s19, v255, 6
	s_mov_b32 s9, 0xf800000
	s_mov_b32 s20, 0x3fd744fd
	s_cbranch_scc1 .LBB0_776
	s_lshl_b32 s22, s30, 10
	v_readlane_b32 s44, v252, 16
	s_lshl_b64 s[2:3], s[22:23], 2
	v_readlane_b32 s46, v252, 18
	v_readlane_b32 s47, v252, 19
	s_add_u32 s4, s46, s2
	s_addc_u32 s5, s47, s3
	v_lshlrev_b32_e32 v1, 3, v0
	v_readlane_b32 s45, v252, 17
	s_add_u32 s2, s44, s2
	v_lshlrev_b32_e32 v2, 4, v0
	v_and_b32_e32 v1, 0x78, v1
	s_movk_i32 s0, 0xff00
	s_addc_u32 s3, s45, s3
	s_waitcnt vmcnt(0)
	v_and_or_b32 v4, v2, s0, v1
	v_ashrrev_i32_e32 v5, 31, v4
	s_add_u32 s22, s38, 0x100000
	v_lshlrev_b64 v[54:55], 2, v[4:5]
	s_addc_u32 s42, s39, 0
	s_ashr_i32 s41, s40, 31
	v_lshl_add_u64 v[56:57], s[2:3], 0, v[54:55]
	v_lshl_add_u64 v[58:59], s[4:5], 0, v[54:55]
	s_lshl_b64 s[2:3], s[40:41], 10
	s_lshl_b64 s[4:5], s[40:41], 11
	v_or_b32_e32 v6, 0x80, v4
	v_lshl_add_u64 v[60:61], s[2:3], 0, v[4:5]
	s_add_u32 s2, s2, 0x52900000
	v_ashrrev_i32_e32 v7, 31, v6
	v_ashrrev_i32_e32 v3, 31, v2
	v_lshlrev_b32_e32 v0, 2, v0
	s_addc_u32 s3, s3, 0
	v_xor_b32_e32 v76, 4, v0
	v_xor_b32_e32 v77, 8, v0
	v_xor_b32_e32 v78, 16, v0
	v_xor_b32_e32 v79, 32, v0
	v_xor_b32_e32 v80, 64, v0
	v_xor_b32_e32 v81, 0x80, v0
	v_lshl_add_u64 v[62:63], v[4:5], 1, s[4:5]
	v_lshl_add_u64 v[64:65], s[2:3], 0, v[2:3]
	v_lshlrev_b64 v[66:67], 2, v[6:7]
	v_readlane_b32 s48, v252, 20
	v_readlane_b32 s49, v252, 21
	v_readlane_b32 s50, v252, 22
	v_readlane_b32 s51, v252, 23
	v_readlane_b32 s52, v252, 24
	v_readlane_b32 s53, v252, 25
	v_readlane_b32 s54, v252, 26
	v_readlane_b32 s55, v252, 27
	v_readlane_b32 s56, v252, 28
	v_readlane_b32 s57, v252, 29
	v_readlane_b32 s58, v252, 30
	v_readlane_b32 s59, v252, 31
	s_brev_b32 s84, 38
	s_mov_b32 s85, 0
	v_lshl_add_u64 v[148:149], s[38:39], 0, v[62:63]
	v_lshl_add_u64 v[148:149], v[148:149], 0, s[84:85]
	v_lshl_add_u64 v[150:151], s[38:39], 0, v[64:65]
	global_load_dwordx4 v[128:131], v[148:149], off nt
	global_load_dwordx4 v[132:135], v[148:149], off offset:256 nt
	global_load_dwordx4 v[144:147], v[150:151], off nt
	global_load_dwordx4 v[156:159], v[56:57], off offset:16
	global_load_dwordx4 v[160:163], v[56:57], off
	global_load_dwordx4 v[164:167], v[58:59], off offset:16
	global_load_dwordx4 v[168:171], v[58:59], off
	global_load_dwordx4 v[172:175], v[56:57], off offset:528
	global_load_dwordx4 v[176:179], v[56:57], off offset:512
	global_load_dwordx4 v[180:183], v[58:59], off offset:528
	global_load_dwordx4 v[184:187], v[58:59], off offset:512
	s_mov_b32 s88, 1
.LBB0_775:
	s_min_i32 s0, s40, 0x10000
	s_ashr_i32 s0, s0, 12
	s_ashr_i32 s2, s0, 31
	s_mul_i32 s3, s30, 17
	s_add_u32 s0, s0, s3
	s_addc_u32 s2, s2, 0
	s_mulk_i32 s2, 0x6000
	s_mul_hi_u32 s3, s0, 0x6000
	s_add_i32 s3, s3, s2
	v_lshl_add_u64 v[2:3], s[38:39], 0, v[62:63]
	s_brev_b32 s2, 38
	v_add_co_u32_e32 v68, vcc, s2, v2
	v_lshl_add_u64 v[0:1], s[38:39], 0, v[64:65]
	s_nop 0
	v_addc_co_u32_e32 v69, vcc, 0, v3, vcc
	s_nop 0
	s_mulk_i32 s0, 0x6000
	s_add_u32 s0, s22, s0
	s_addc_u32 s4, s42, s3
	s_add_u32 s2, s0, 0x2000
	s_addc_u32 s3, s4, 0
	s_add_u32 s36, s0, 0x3000
	s_addc_u32 s37, s4, 0
	v_lshl_add_u64 v[62:63], v[62:63], 0, s[18:19]
	v_lshl_add_u64 v[64:65], v[64:65], 0, s[10:11]
	s_cmp_eq_u32 s0, s88
	s_cbranch_scc1 .Lln1_md_keep
	s_mov_b32 s88, s0
	s_add_u32 s90, s0, 0x4000
	s_addc_u32 s91, s4, 0
	v_lshl_add_u64 v[236:237], s[2:3], 0, v[54:55]
	v_lshl_add_u64 v[238:239], s[2:3], 0, v[66:67]
	v_lshl_add_u64 v[240:241], s[36:37], 0, v[54:55]
	v_lshl_add_u64 v[242:243], s[36:37], 0, v[66:67]
	v_lshl_add_u64 v[244:245], s[90:91], 0, v[54:55]
	v_lshl_add_u64 v[246:247], s[90:91], 0, v[66:67]
	global_load_dwordx4 v[136:139], v[236:237], off
	global_load_dwordx4 v[140:143], v[236:237], off offset:16
	global_load_dwordx4 v[152:155], v[238:239], off
	global_load_dwordx4 v[188:191], v[238:239], off offset:16
	global_load_dwordx4 v[194:197], v[240:241], off offset:16
	global_load_dwordx4 v[198:201], v[240:241], off
	global_load_dwordx4 v[202:205], v[244:245], off offset:16
	global_load_dwordx4 v[206:209], v[244:245], off
	global_load_dwordx4 v[210:213], v[242:243], off offset:16
	global_load_dwordx4 v[214:217], v[242:243], off
	global_load_dwordx4 v[218:221], v[246:247], off offset:16
	global_load_dwordx4 v[222:225], v[246:247], off
; #define GAS __attribute__((address_space(1)))
; __device__ __forceinline__ void unpack8(const u32x4 q, float* o) { o[0] = bflo(q.x); o[1] = bfhi(q.x); o[2] = bflo(q.y); o[3] = bfhi(q.y); o[4] = bflo(q.z); o[5] = bfhi(q.z); o[6] = bflo(q.w); o[7] = bfhi(q.w); }
; __device__ __forceinline__ void ph_ln1(Frame& F, int l, int ntok) {
;     ...
;         const u32x4 xa = __builtin_nontemporal_load((const GAS u32x4*)(xr + cA)), xb = __builtin_nontemporal_load((const GAS u32x4*)(xr + cA + 128)), ya = __builtin_nontemporal_load((const GAS u32x4*)yr);
;         float x[16], y[16], v[16]; unpack8(xa, x); unpack8(xb, x + 8);
;         { const unsigned a[4] = {ya.x, ya.y, ya.z, ya.w};
; #pragma unroll
;           for (int e = 0; e < 4; ++e) { const f32x2 lo = __builtin_amdgcn_cvt_pk_f32_fp8((int)a[e], false), hi = __builtin_amdgcn_cvt_pk_f32_fp8((int)a[e], true); y[4 * e] = lo.x; y[4 * e + 1] = lo.y; y[4 * e + 2] = hi.x; y[4 * e + 3] = hi.y; } }
;         float s = 0.f;
; #pragma unroll
;         for (int j = 0; j < 4; ++j) { const f32x4 g1 = *(const GAS f32x4*)(md + 2048 + LN1_COL(j));
; #pragma unroll
;             for (int e = 0; e < 4; ++e) { v[4 * j + e] = x[4 * j + e] * DN_ALPHA + g1[e] * y[4 * j + e]; s += v[4 * j + e]; } }
;         const float mean = wave_sum(s, F.lane) * (1.f / DM); float s2 = 0.f;
; #pragma unroll
;         for (int e = 0; e < 16; ++e) { v[e] -= mean; s2 += v[e] * v[e]; }
;         const float rstd = 1.f / sqrtf(wave_sum(s2, F.lane) * (1.f / DM) + LN_EPS);
;         unsigned wx[8]; int w8[4];
; #pragma unroll
;         for (int j = 0; j < 4; ++j) { const f32x4 g = *(const GAS f32x4*)(lg + LN1_COL(j)), bb = *(const GAS f32x4*)(lb + LN1_COL(j)), sh = *(const GAS f32x4*)(md + 3072 + LN1_COL(j)), sc = *(const GAS f32x4*)(md + 4096 + LN1_COL(j));
.Lln1_md_keep:
	s_waitcnt vmcnt(0)
	v_mov_b32_e32 v46, v128
	v_mov_b32_e32 v47, v129
	v_mov_b32_e32 v48, v130
	v_mov_b32_e32 v49, v131
	v_mov_b32_e32 v90, v132
	v_mov_b32_e32 v91, v133
	v_mov_b32_e32 v92, v134
	v_mov_b32_e32 v93, v135
	v_mov_b32_e32 v0, v144
	v_mov_b32_e32 v1, v145
	v_mov_b32_e32 v2, v146
	v_mov_b32_e32 v3, v147
	v_lshlrev_b32_e32 v122, 16, v93
	v_cvt_pk_f32_fp8_e32 v[24:25], v0
	v_cvt_pk_f32_fp8_sdwa v[70:71], v0 src0_sel:WORD_1
	v_cvt_pk_f32_fp8_e32 v[72:73], v1
	v_cvt_pk_f32_fp8_sdwa v[74:75], v1 src0_sel:WORD_1
	v_lshl_add_u64 v[0:1], s[2:3], 0, v[54:55]
	v_mov_b32_e32 v50, v136
	v_mov_b32_e32 v51, v137
	v_mov_b32_e32 v52, v138
	v_mov_b32_e32 v53, v139
	v_mov_b32_e32 v94, v140
	v_mov_b32_e32 v95, v141
	v_mov_b32_e32 v96, v142
	v_mov_b32_e32 v97, v143
	v_lshl_add_u64 v[0:1], s[2:3], 0, v[66:67]
	v_mov_b32_e32 v98, v152
	v_mov_b32_e32 v99, v153
	v_mov_b32_e32 v100, v154
	v_mov_b32_e32 v101, v155
	v_mov_b32_e32 v102, v188
	v_mov_b32_e32 v103, v189
	v_mov_b32_e32 v104, v190
	v_mov_b32_e32 v105, v191
	s_add_u32 s2, s0, 0x4000
	s_addc_u32 s3, s4, 0
	v_lshl_add_u64 v[0:1], s[36:37], 0, v[54:55]
	v_lshl_add_u64 v[4:5], s[2:3], 0, v[54:55]
	v_cvt_pk_f32_fp8_e32 v[114:115], v2
	v_cvt_pk_f32_fp8_sdwa v[116:117], v2 src0_sel:WORD_1
	v_cvt_pk_f32_fp8_e32 v[118:119], v3
	v_cvt_pk_f32_fp8_sdwa v[120:121], v3 src0_sel:WORD_1
	v_mov_b32_e32 v26, v156
	v_mov_b32_e32 v27, v157
	v_mov_b32_e32 v28, v158
	v_mov_b32_e32 v29, v159
	v_mov_b32_e32 v106, v160
	v_mov_b32_e32 v107, v161
	v_mov_b32_e32 v108, v162
	v_mov_b32_e32 v109, v163
	v_mov_b32_e32 v30, v164
	v_mov_b32_e32 v31, v165
	v_mov_b32_e32 v32, v166
	v_mov_b32_e32 v33, v167
	v_mov_b32_e32 v110, v168
	v_mov_b32_e32 v111, v169
	v_mov_b32_e32 v112, v170
	v_mov_b32_e32 v113, v171
	v_mov_b32_e32 v12, v194
	v_mov_b32_e32 v13, v195
	v_mov_b32_e32 v14, v196
	v_mov_b32_e32 v15, v197
	v_mov_b32_e32 v42, v198
	v_mov_b32_e32 v43, v199
	v_mov_b32_e32 v44, v200
	v_mov_b32_e32 v45, v201
	s_nop 0
	v_mov_b32_e32 v0, v202
	v_mov_b32_e32 v1, v203
	v_mov_b32_e32 v2, v204
	v_mov_b32_e32 v3, v205
	s_nop 0
	v_mov_b32_e32 v4, v206
	v_mov_b32_e32 v5, v207
	v_mov_b32_e32 v6, v208
	v_mov_b32_e32 v7, v209
	v_and_b32_e32 v123, 0xffff0000, v93
	v_lshl_add_u64 v[82:83], s[2:3], 0, v[66:67]
	s_waitcnt lgkmcnt(0)
	v_mov_b32_e32 v8, v172
	v_mov_b32_e32 v9, v173
	v_mov_b32_e32 v10, v174
	v_mov_b32_e32 v11, v175
	v_mov_b32_e32 v34, v176
	v_mov_b32_e32 v35, v177
	v_mov_b32_e32 v36, v178
	v_mov_b32_e32 v37, v179
	v_mov_b32_e32 v16, v180
	v_mov_b32_e32 v17, v181
	v_mov_b32_e32 v18, v182
	v_mov_b32_e32 v19, v183
	v_mov_b32_e32 v38, v184
	v_mov_b32_e32 v39, v185
	v_mov_b32_e32 v40, v186
	v_mov_b32_e32 v41, v187
	s_mov_b32 s0, 0x5be00000
	s_add_i32 s40, s40, s8
	s_cmp_lt_i32 s40, s80
	s_waitcnt vmcnt(0)
	v_pk_mul_f32 v[52:53], v[70:71], v[52:53]
	v_lshlrev_b32_e32 v70, 16, v46
	v_and_b32_e32 v71, 0xffff0000, v46
	v_pk_mul_f32 v[24:25], v[24:25], v[50:51]
	s_waitcnt vmcnt(0)
	v_pk_mul_f32 v[104:105], v[120:121], v[104:105]
	v_lshlrev_b32_e32 v120, 16, v92
	v_and_b32_e32 v121, 0xffff0000, v92
	v_pk_mul_f32 v[92:93], v[118:119], v[102:103]
	v_lshlrev_b32_e32 v102, 16, v91
	v_and_b32_e32 v103, 0xffff0000, v91
	v_pk_mul_f32 v[100:101], v[116:117], v[100:101]
	v_pk_fma_f32 v[24:25], v[70:71], s[20:21], v[24:25] op_sel_hi:[1,0,1]
	v_pk_fma_f32 v[100:101], v[102:103], s[20:21], v[100:101] op_sel_hi:[1,0,1]
	v_lshlrev_b32_e32 v102, 16, v90
	v_and_b32_e32 v103, 0xffff0000, v90
	v_pk_mul_f32 v[90:91], v[114:115], v[98:99]
	v_lshlrev_b32_e32 v98, 16, v49
	v_and_b32_e32 v99, 0xffff0000, v49
	v_pk_mul_f32 v[74:75], v[74:75], v[96:97]
	v_lshlrev_b32_e32 v96, 16, v48
	v_and_b32_e32 v97, 0xffff0000, v48
	v_pk_mul_f32 v[48:49], v[72:73], v[94:95]
	v_lshlrev_b32_e32 v72, 16, v47
	v_and_b32_e32 v73, 0xffff0000, v47
	v_add_f32_e32 v46, 0, v24
	v_pk_fma_f32 v[52:53], v[72:73], s[20:21], v[52:53] op_sel_hi:[1,0,1]
	v_add_f32_e32 v46, v25, v46
	v_add_f32_e32 v46, v52, v46
	v_pk_fma_f32 v[48:49], v[96:97], s[20:21], v[48:49] op_sel_hi:[1,0,1]
	v_add_f32_e32 v46, v53, v46
	v_add_f32_e32 v46, v48, v46
	v_pk_fma_f32 v[74:75], v[98:99], s[20:21], v[74:75] op_sel_hi:[1,0,1]
	v_add_f32_e32 v46, v49, v46
	v_add_f32_e32 v46, v74, v46
	v_pk_fma_f32 v[90:91], v[102:103], s[20:21], v[90:91] op_sel_hi:[1,0,1]
	v_add_f32_e32 v46, v75, v46
	v_add_f32_e32 v46, v90, v46
	v_add_f32_e32 v46, v91, v46
	v_add_f32_e32 v46, v100, v46
	v_pk_fma_f32 v[92:93], v[120:121], s[20:21], v[92:93] op_sel_hi:[1,0,1]
	v_add_f32_e32 v46, v101, v46
	v_add_f32_e32 v46, v92, v46
	v_pk_fma_f32 v[104:105], v[122:123], s[20:21], v[104:105] op_sel_hi:[1,0,1]
	v_add_f32_e32 v46, v93, v46
	v_add_f32_e32 v46, v104, v46
	v_add_f32_e32 v46, v105, v46
	ds_bpermute_b32 v47, v76, v46
	s_waitcnt vmcnt(0)
	v_add_f32_e32 v124, 1.0, v4
	v_add_f32_e32 v125, 1.0, v5
	v_lshl_add_u64 v[4:5], s[36:37], 0, v[66:67]
	v_add_f32_e32 v126, 1.0, v6
	s_waitcnt lgkmcnt(0)
	v_add_f32_e32 v46, v46, v47
	ds_bpermute_b32 v47, v77, v46
	v_add_f32_e32 v127, 1.0, v7
	v_add_f32_e32 v86, 1.0, v0
	v_add_f32_e32 v87, 1.0, v1
	v_add_f32_e32 v88, 1.0, v2
	s_waitcnt lgkmcnt(0)
	v_add_f32_e32 v46, v46, v47
	ds_bpermute_b32 v47, v78, v46
	v_add_f32_e32 v89, 1.0, v3
	v_mov_b32_e32 v0, v210
	v_mov_b32_e32 v1, v211
	v_mov_b32_e32 v2, v212
	v_mov_b32_e32 v3, v213
	v_mov_b32_e32 v20, v214
	v_mov_b32_e32 v21, v215
	v_mov_b32_e32 v22, v216
	v_mov_b32_e32 v23, v217
	s_nop 0
	v_mov_b32_e32 v4, v218
	v_mov_b32_e32 v5, v219
	v_mov_b32_e32 v6, v220
	v_mov_b32_e32 v7, v221
	s_nop 0
	v_mov_b32_e32 v82, v222
	v_mov_b32_e32 v83, v223
	v_mov_b32_e32 v84, v224
	v_mov_b32_e32 v85, v225
	s_cselect_b64 s[86:87], -1, 0
	v_lshl_add_u64 v[148:149], s[38:39], 0, v[62:63]
	v_lshl_add_u64 v[148:149], v[148:149], 0, s[84:85]
	v_lshl_add_u64 v[150:151], s[38:39], 0, v[64:65]
	v_cndmask_b32_e64 v148, v68, v148, s[86:87]
	v_cndmask_b32_e64 v149, v69, v149, s[86:87]
	v_cndmask_b32_e64 v150, v68, v150, s[86:87]
	v_cndmask_b32_e64 v151, v69, v151, s[86:87]
	global_load_dwordx4 v[128:131], v[148:149], off nt
	global_load_dwordx4 v[132:135], v[148:149], off offset:256 nt
	global_load_dwordx4 v[144:147], v[150:151], off nt
	s_waitcnt lgkmcnt(0)
; #define GAS __attribute__((address_space(1)))
; __device__ __forceinline__ unsigned pk2(float lo, float hi) { const f32x2 v = {lo, hi}; const bf16v2 b = __builtin_convertvector(v, bf16v2); return __builtin_bit_cast(unsigned, b); }
; __device__ __forceinline__ void ph_ln1(Frame& F, int l, int ntok) {
;     ...
;         const float mean = wave_sum(s, F.lane) * (1.f / DM); float s2 = 0.f;
; #pragma unroll
;         for (int e = 0; e < 16; ++e) { v[e] -= mean; s2 += v[e] * v[e]; }
;         const float rstd = 1.f / sqrtf(wave_sum(s2, F.lane) * (1.f / DM) + LN_EPS);
;         unsigned wx[8]; int w8[4];
; #pragma unroll
;         for (int j = 0; j < 4; ++j) { const f32x4 g = *(const GAS f32x4*)(lg + LN1_COL(j)), bb = *(const GAS f32x4*)(lb + LN1_COL(j)), sh = *(const GAS f32x4*)(md + 3072 + LN1_COL(j)), sc = *(const GAS f32x4*)(md + 4096 + LN1_COL(j));
;             float xn[4];
; #pragma unroll
;             for (int e = 0; e < 4; ++e) xn[e] = v[4 * j + e] * rstd * g[e] + bb[e];
;             wx[2 * j] = pk2(xn[0], xn[1]); wx[2 * j + 1] = pk2(xn[2], xn[3]);
;             const float h0 = xn[0] * (1.f + sc[0]) + sh[0], h1 = xn[1] * (1.f + sc[1]) + sh[1], h2 = xn[2] * (1.f + sc[2]) + sh[2], h3 = xn[3] * (1.f + sc[3]) + sh[3];
;             int v = 0; v = __builtin_amdgcn_cvt_pk_fp8_f32(h0, h1, v, false); v = __builtin_amdgcn_cvt_pk_fp8_f32(h2, h3, v, true); w8[j] = v; }
;         unsigned char* x8 = (unsigned char*)(F.ws + WS_XM8) + (size_t)row * DM;
;         __builtin_nontemporal_store((u32x2){(unsigned)w8[0], (unsigned)w8[1]}, (GAS u32x2*)(x8 + cA)); __builtin_nontemporal_store((u32x2){(unsigned)w8[2], (unsigned)w8[3]}, (GAS u32x2*)(x8 + cA + 128));
;         __builtin_nontemporal_store((u32x4){wx[0], wx[1], wx[2], wx[3]}, (GAS u32x4*)(xr + cA)); __builtin_nontemporal_store((u32x4){wx[4], wx[5], wx[6], wx[7]}, (GAS u32x4*)(xr + cA + 128));
	v_add_f32_e32 v46, v46, v47
	ds_bpermute_b32 v47, v79, v46
	s_waitcnt lgkmcnt(0)
	v_add_f32_e32 v46, v46, v47
	ds_bpermute_b32 v47, v80, v46
	s_waitcnt lgkmcnt(0)
	v_add_f32_e32 v46, v46, v47
	ds_bpermute_b32 v47, v81, v46
	s_waitcnt lgkmcnt(0)
	v_add_f32_e32 v46, v46, v47
	v_mul_f32_e32 v50, 0x3a800000, v46
	v_pk_add_f32 v[24:25], v[24:25], v[50:51] op_sel_hi:[1,0] neg_lo:[0,1] neg_hi:[0,1]
	v_pk_add_f32 v[96:97], v[52:53], v[50:51] op_sel_hi:[1,0] neg_lo:[0,1] neg_hi:[0,1]
	v_pk_mul_f32 v[94:95], v[24:25], v[24:25]
	v_pk_mul_f32 v[98:99], v[96:97], v[96:97]
	v_add_f32_e32 v94, v94, v95
	v_pk_add_f32 v[72:73], v[48:49], v[50:51] op_sel_hi:[1,0] neg_lo:[0,1] neg_hi:[0,1]
	v_add_f32_e32 v94, v98, v94
	v_pk_mul_f32 v[102:103], v[72:73], v[72:73]
	v_add_f32_e32 v94, v99, v94
	v_pk_add_f32 v[74:75], v[74:75], v[50:51] op_sel_hi:[1,0] neg_lo:[0,1] neg_hi:[0,1]
	v_add_f32_e32 v94, v102, v94
	v_pk_mul_f32 v[114:115], v[74:75], v[74:75]
	v_add_f32_e32 v94, v103, v94
	v_pk_add_f32 v[52:53], v[90:91], v[50:51] op_sel_hi:[1,0] neg_lo:[0,1] neg_hi:[0,1]
	v_add_f32_e32 v94, v114, v94
	v_pk_mul_f32 v[90:91], v[52:53], v[52:53]
	v_add_f32_e32 v94, v115, v94
	v_pk_add_f32 v[70:71], v[100:101], v[50:51] op_sel_hi:[1,0] neg_lo:[0,1] neg_hi:[0,1]
	v_add_f32_e32 v90, v90, v94
	v_pk_mul_f32 v[100:101], v[70:71], v[70:71]
	v_add_f32_e32 v90, v91, v90
	v_pk_add_f32 v[46:47], v[92:93], v[50:51] op_sel_hi:[1,0] neg_lo:[0,1] neg_hi:[0,1]
	v_add_f32_e32 v90, v100, v90
	v_pk_mul_f32 v[92:93], v[46:47], v[46:47]
	v_add_f32_e32 v90, v101, v90
	v_pk_add_f32 v[48:49], v[104:105], v[50:51] op_sel_hi:[1,0] neg_lo:[0,1] neg_hi:[0,1]
	v_add_f32_e32 v90, v92, v90
	v_pk_mul_f32 v[50:51], v[48:49], v[48:49]
	v_add_f32_e32 v90, v93, v90
	v_add_f32_e32 v50, v50, v90
	v_add_f32_e32 v50, v51, v50
	ds_bpermute_b32 v51, v76, v50
	s_waitcnt lgkmcnt(0)
	v_add_f32_e32 v50, v50, v51
	ds_bpermute_b32 v51, v77, v50
	s_waitcnt lgkmcnt(0)
	v_add_f32_e32 v50, v50, v51
	ds_bpermute_b32 v51, v78, v50
	s_waitcnt lgkmcnt(0)
	v_add_f32_e32 v50, v50, v51
	ds_bpermute_b32 v51, v79, v50
	s_waitcnt lgkmcnt(0)
	v_add_f32_e32 v50, v50, v51
	ds_bpermute_b32 v51, v80, v50
	s_waitcnt vmcnt(3)
	v_add_f32_e32 v4, 1.0, v4
	s_waitcnt vmcnt(3)
	v_add_f32_e32 v82, 1.0, v82
	v_add_f32_e32 v83, 1.0, v83
	s_waitcnt lgkmcnt(0)
	v_add_f32_e32 v50, v50, v51
	ds_bpermute_b32 v51, v81, v50
	v_add_f32_e32 v84, 1.0, v84
	v_add_f32_e32 v85, 1.0, v85
	s_waitcnt lgkmcnt(0)
	v_add_f32_e32 v50, v50, v51
	v_fmamk_f32 v50, v50, 0x3a800000, v234
	v_cmp_gt_f32_e32 vcc, s9, v50
	v_mul_f32_e32 v51, 0x4f800000, v50
	s_nop 0
	v_cndmask_b32_e32 v50, v50, v51, vcc
	v_sqrt_f32_e32 v51, v50
	s_nop 0
	v_add_u32_e32 v90, -1, v51
	v_fma_f32 v91, -v90, v51, v50
	v_cmp_ge_f32_e64 s[36:37], 0, v91
	v_add_u32_e32 v91, 1, v51
	s_nop 0
	v_cndmask_b32_e64 v90, v51, v90, s[36:37]
	v_fma_f32 v51, -v91, v51, v50
	v_cmp_lt_f32_e64 s[36:37], 0, v51
	s_nop 1
	v_cndmask_b32_e64 v51, v90, v91, s[36:37]
	v_mul_f32_e32 v90, 0x37800000, v51
	v_cndmask_b32_e32 v51, v51, v90, vcc
	v_cmp_class_f32_e32 vcc, v50, v232
	s_nop 1
	v_cndmask_b32_e32 v50, v51, v50, vcc
	v_div_scale_f32 v51, s[2:3], v50, v50, 1.0
	v_rcp_f32_e32 v90, v51
	s_nop 0
	v_fma_f32 v91, -v51, v90, 1.0
	v_fmac_f32_e32 v90, v91, v90
	v_div_scale_f32 v91, vcc, 1.0, v50, 1.0
	v_mul_f32_e32 v92, v91, v90
	v_fma_f32 v93, -v51, v92, v91
	v_fmac_f32_e32 v92, v93, v90
	v_fma_f32 v51, -v51, v92, v91
	v_div_fmas_f32 v51, v51, v90, v92
	v_div_fixup_f32 v50, v51, v50, 1.0
	v_pk_mul_f32 v[24:25], v[24:25], v[50:51] op_sel_hi:[1,0]
	s_nop 0
	v_pk_fma_f32 v[90:91], v[106:107], v[24:25], v[110:111]
	v_pk_mul_f32 v[24:25], v[96:97], v[50:51] op_sel_hi:[1,0]
	v_fma_f32 v42, v124, v90, v42
	v_pk_fma_f32 v[92:93], v[108:109], v[24:25], v[112:113]
	v_cvt_pk_bf16_f32 v24, v90, v91
	v_fma_f32 v43, v125, v91, v43
	v_mov_b32_e32 v90, v193
	v_cvt_pk_fp8_f32 v90, v42, v43
	v_pk_mul_f32 v[42:43], v[72:73], v[50:51] op_sel_hi:[1,0]
	v_mov_b32_e32 v91, v193
	v_pk_fma_f32 v[30:31], v[26:27], v[42:43], v[30:31]
	v_pk_mul_f32 v[26:27], v[74:75], v[50:51] op_sel_hi:[1,0]
	v_fma_f32 v12, v86, v30, v12
	v_fma_f32 v13, v87, v31, v13
	v_cvt_pk_fp8_f32 v91, v12, v13
	v_pk_fma_f32 v[28:29], v[28:29], v[26:27], v[32:33]
	v_pk_mul_f32 v[12:13], v[52:53], v[50:51] op_sel_hi:[1,0]
	v_fma_f32 v14, v88, v28, v14
	v_fmac_f32_e32 v15, v89, v29
	v_cvt_pk_fp8_f32 v91, v14, v15 op_sel:[0,0,1]
	v_pk_fma_f32 v[14:15], v[34:35], v[12:13], v[38:39]
	v_pk_mul_f32 v[12:13], v[70:71], v[50:51] op_sel_hi:[1,0]
	v_cvt_pk_bf16_f32 v27, v28, v29
	v_pk_fma_f32 v[28:29], v[36:37], v[12:13], v[40:41]
	v_cvt_pk_bf16_f32 v12, v14, v15
	v_fma_f32 v14, v82, v14, v20
	v_fma_f32 v15, v83, v15, v21
	v_mov_b32_e32 v20, v193
	v_cvt_pk_fp8_f32 v20, v14, v15
	v_pk_mul_f32 v[14:15], v[46:47], v[50:51] op_sel_hi:[1,0]
	v_fma_f32 v21, v84, v28, v22
	v_pk_fma_f32 v[8:9], v[8:9], v[14:15], v[16:17]
	v_fmac_f32_e32 v23, v85, v29
	v_fma_f32 v0, v4, v8, v0
	v_add_f32_e32 v4, 1.0, v5
	v_cvt_pk_fp8_f32 v20, v21, v23 op_sel:[0,0,1]
	v_fma_f32 v1, v4, v9, v1
	v_mov_b32_e32 v21, v193
	v_pk_mul_f32 v[14:15], v[48:49], v[50:51] op_sel_hi:[1,0]
	v_cvt_pk_fp8_f32 v21, v0, v1
	v_pk_fma_f32 v[10:11], v[10:11], v[14:15], v[18:19]
	v_add_f32_e32 v4, 1.0, v6
	v_fma_f32 v44, v126, v92, v44
	v_fmac_f32_e32 v45, v127, v93
	v_fma_f32 v2, v4, v10, v2
	v_add_f32_e32 v4, 1.0, v7
	v_cvt_pk_fp8_f32 v90, v44, v45 op_sel:[0,0,1]
	v_fmac_f32_e32 v3, v4, v11
	v_cvt_pk_fp8_f32 v21, v2, v3 op_sel:[0,0,1]
	v_lshl_add_u64 v[0:1], s[38:39], 0, v[60:61]
	v_add_co_u32_e32 v0, vcc, s0, v0
	v_lshl_add_u64 v[60:61], v[60:61], 0, s[10:11]
	s_nop 0
	v_addc_co_u32_e32 v1, vcc, 0, v1, vcc
	v_cvt_pk_bf16_f32 v25, v92, v93
	v_cvt_pk_bf16_f32 v26, v30, v31
	v_cvt_pk_bf16_f32 v13, v28, v29
	v_cvt_pk_bf16_f32 v14, v8, v9
	v_cvt_pk_bf16_f32 v15, v10, v11
	global_store_dwordx2 v[0:1], v[90:91], off nt
	global_store_dwordx2 v[0:1], v[20:21], off offset:128 nt
	global_store_dwordx4 v[68:69], v[24:27], off nt
	global_store_dwordx4 v[68:69], v[12:15], off offset:256 nt
	s_cbranch_scc1 .LBB0_775
